# L1+L2: batch the 9 serialized CSR index loads per task into one wait (nested exec masks)
# speedup vs baseline: 1.0304x; 1.0304x over previous
.LBB4_24:
	s_or_b64 exec, exec, s[6:7]
	s_waitcnt vmcnt(0)
	v_sub_u32_e32 v72, v33, v32
	v_sub_u32_e32 v108, v34, v33
	v_sub_u32_e32 v35, v35, v34
	v_add_lshl_u32 v37, v32, v97, 2
	v_add_lshl_u32 v38, v33, v97, 2
	v_add_lshl_u32 v39, v34, v97, 2
	v_mov_b32_e32 v36, 0x4000000
	v_mov_b32_e32 v68, 0x4000000
	v_mov_b32_e32 v74, 0x4000000
	v_mov_b32_e32 v85, 0x4000000
	v_mov_b32_e32 v84, 0x4000000
	v_mov_b32_e32 v109, 0x4000000
	v_mov_b32_e32 v107, 0x4000000
	v_mov_b32_e32 v106, 0x4000000
	v_mov_b32_e32 v95, 0x4000000
	s_mov_b64 s[6:7], exec
	v_cmp_lt_i32_e32 vcc, v97, v72
	s_and_b64 exec, exec, vcc
	global_load_dword v36, v37, s[12:13]
	v_cmp_lt_i32_e32 vcc, v100, v72
	s_and_b64 exec, exec, vcc
	global_load_dword v68, v37, s[12:13] offset:32
	v_cmp_lt_i32_e32 vcc, v101, v72
	s_and_b64 exec, exec, vcc
	global_load_dword v74, v37, s[12:13] offset:64
	s_mov_b64 exec, s[6:7]
	v_cmp_lt_i32_e32 vcc, v97, v108
	s_and_b64 exec, exec, vcc
	global_load_dword v85, v38, s[12:13]
	v_cmp_lt_i32_e32 vcc, v100, v108
	s_and_b64 exec, exec, vcc
	global_load_dword v84, v38, s[12:13] offset:32
	v_cmp_lt_i32_e32 vcc, v101, v108
	s_and_b64 exec, exec, vcc
	global_load_dword v109, v38, s[12:13] offset:64
	s_mov_b64 exec, s[6:7]
	v_cmp_lt_i32_e32 vcc, v97, v35
	s_and_b64 exec, exec, vcc
	global_load_dword v107, v39, s[12:13]
	v_cmp_lt_i32_e32 vcc, v100, v35
	s_and_b64 exec, exec, vcc
	global_load_dword v106, v39, s[12:13] offset:32
	v_cmp_lt_i32_e32 vcc, v101, v35
	s_and_b64 exec, exec, vcc
	global_load_dword v95, v39, s[12:13] offset:64
	s_mov_b64 exec, s[6:7]
	s_waitcnt vmcnt(0)
	v_lshrrev_b32_e32 v36, 10, v36
	v_lshrrev_b32_e32 v68, 10, v68
	v_lshrrev_b32_e32 v74, 10, v74
	v_lshrrev_b32_e32 v85, 10, v85
	v_lshrrev_b32_e32 v84, 10, v84
	v_lshrrev_b32_e32 v109, 10, v109
	v_lshrrev_b32_e32 v107, 10, v107
	v_lshrrev_b32_e32 v106, 10, v106
	v_lshrrev_b32_e32 v95, 10, v95
	v_and_b32_e32 v36, 0x3fff80, v36
	v_and_b32_e32 v68, 0x3fff80, v68
	v_and_b32_e32 v74, 0x3fff80, v74
	v_and_b32_e32 v85, 0x3fff80, v85
	v_and_b32_e32 v84, 0x3fff80, v84
	v_and_b32_e32 v109, 0x3fff80, v109
	v_and_b32_e32 v107, 0x3fff80, v107
	v_and_b32_e32 v106, 0x3fff80, v106
	v_and_b32_e32 v95, 0x3fff80, v95
	ds_swizzle_b32 v37, v36 offset:swizzle(BROADCAST,8,0)
	ds_swizzle_b32 v38, v36 offset:swizzle(BROADCAST,8,1)
	ds_swizzle_b32 v39, v36 offset:swizzle(BROADCAST,8,2)
	ds_swizzle_b32 v40, v36 offset:swizzle(BROADCAST,8,3)
	ds_swizzle_b32 v41, v36 offset:swizzle(BROADCAST,8,6)
	s_waitcnt lgkmcnt(4)
	v_add_u32_e32 v37, v102, v37
	s_waitcnt lgkmcnt(3)
	v_add_u32_e32 v38, v102, v38
	ds_read_b128 v[60:63], v37 offset:52240
	ds_read_b128 v[52:55], v38 offset:52240
	s_waitcnt lgkmcnt(4)
	v_add_u32_e32 v37, v102, v39
	ds_swizzle_b32 v38, v36 offset:swizzle(BROADCAST,8,4)
	s_waitcnt lgkmcnt(4)
	v_add_u32_e32 v39, v102, v40
	ds_swizzle_b32 v40, v36 offset:swizzle(BROADCAST,8,5)
	ds_swizzle_b32 v42, v36 offset:swizzle(BROADCAST,8,7)
	ds_read_b128 v[64:67], v37 offset:52240
	ds_read_b128 v[56:59], v39 offset:52240
	s_waitcnt lgkmcnt(4)
	v_add_u32_e32 v37, v102, v38
	v_cmp_lt_i32_e32 vcc, 8, v72
	s_waitcnt lgkmcnt(3)
	v_add_u32_e32 v36, v102, v40
	v_add_u32_e32 v40, v102, v41
	s_waitcnt lgkmcnt(2)
	v_add_u32_e32 v41, v102, v42
	ds_read_b128 v[44:47], v37 offset:52240
	ds_read_b128 v[36:39], v36 offset:52240
	ds_read_b128 v[48:51], v40 offset:52240
	ds_read_b128 v[40:43], v41 offset:52240
	s_cmp_lg_u64 vcc, 0
	s_cselect_b64 s[22:23], -1, 0
	v_cmp_lt_i32_e64 s[6:7], 12, v72
	s_cbranch_vccz .LBB4_44
	ds_swizzle_b32 v0, v68 offset:swizzle(BROADCAST,8,0)
	ds_swizzle_b32 v1, v68 offset:swizzle(BROADCAST,8,1)
	ds_swizzle_b32 v16, v68 offset:swizzle(BROADCAST,8,2)
	ds_swizzle_b32 v17, v68 offset:swizzle(BROADCAST,8,3)
	s_waitcnt lgkmcnt(3)
	v_add_u32_e32 v0, v102, v0
	s_waitcnt lgkmcnt(2)
	v_add_u32_e32 v8, v102, v1
	s_waitcnt lgkmcnt(1)
	v_add_u32_e32 v16, v102, v16
	s_waitcnt lgkmcnt(0)
	v_add_u32_e32 v24, v102, v17
	ds_read_b128 v[0:3], v0 offset:52240
	ds_read_b128 v[8:11], v8 offset:52240
	ds_read_b128 v[16:19], v16 offset:52240
	ds_read_b128 v[24:27], v24 offset:52240

.LBB4_105:
	s_branch .LBB4_13
	.p2align	8

.LBB5_22:
	s_or_b64 exec, exec, s[6:7]
	s_waitcnt vmcnt(1)
	v_sub_u32_e32 v58, v5, v4
	v_sub_u32_e32 v87, v6, v5
	v_sub_u32_e32 v85, v7, v6
	v_add_lshl_u32 v10, v4, v75, 2
	v_add_lshl_u32 v11, v5, v75, 2
	v_add_lshl_u32 v12, v6, v75, 2
	v_mov_b32_e32 v9, 0x186a0
	v_mov_b32_e32 v8, 0x186a0
	v_mov_b32_e32 v60, 0x186a0
	v_mov_b32_e32 v59, 0x186a0
	v_mov_b32_e32 v62, 0x186a0
	v_mov_b32_e32 v89, 0x186a0
	v_mov_b32_e32 v88, 0x186a0
	v_mov_b32_e32 v86, 0x186a0
	v_mov_b32_e32 v7, 0x186a0
	s_mov_b64 s[6:7], exec
	v_cmp_lt_i32_e32 vcc, v75, v58
	s_and_b64 exec, exec, vcc
	global_load_dword v9, v10, s[26:27]
	v_cmp_lt_i32_e32 vcc, v78, v58
	s_and_b64 exec, exec, vcc
	global_load_dword v8, v10, s[26:27] offset:32
	v_cmp_lt_i32_e32 vcc, v79, v58
	s_and_b64 exec, exec, vcc
	global_load_dword v60, v10, s[26:27] offset:64
	s_mov_b64 exec, s[6:7]
	v_cmp_lt_i32_e32 vcc, v75, v87
	s_and_b64 exec, exec, vcc
	global_load_dword v59, v11, s[26:27]
	v_cmp_lt_i32_e32 vcc, v78, v87
	s_and_b64 exec, exec, vcc
	global_load_dword v62, v11, s[26:27] offset:32
	v_cmp_lt_i32_e32 vcc, v79, v87
	s_and_b64 exec, exec, vcc
	global_load_dword v89, v11, s[26:27] offset:64
	s_mov_b64 exec, s[6:7]
	v_cmp_lt_i32_e32 vcc, v75, v85
	s_and_b64 exec, exec, vcc
	global_load_dword v88, v12, s[26:27]
	v_cmp_lt_i32_e32 vcc, v78, v85
	s_and_b64 exec, exec, vcc
	global_load_dword v86, v12, s[26:27] offset:32
	v_cmp_lt_i32_e32 vcc, v79, v85
	s_and_b64 exec, exec, vcc
	global_load_dword v7, v12, s[26:27] offset:64
	s_mov_b64 exec, s[6:7]
	s_waitcnt vmcnt(0)
	v_lshlrev_b32_e32 v9, 6, v9
	v_lshlrev_b32_e32 v8, 6, v8
	v_lshlrev_b32_e32 v60, 6, v60
	v_lshlrev_b32_e32 v59, 6, v59
	v_lshlrev_b32_e32 v62, 6, v62
	v_lshlrev_b32_e32 v89, 6, v89
	v_lshlrev_b32_e32 v88, 6, v88
	v_lshlrev_b32_e32 v86, 6, v86
	v_lshlrev_b32_e32 v7, 6, v7
	v_and_b32_e32 v9, 0x7fffc0, v9
	v_and_b32_e32 v8, 0x7fffc0, v8
	v_and_b32_e32 v60, 0x7fffc0, v60
	v_and_b32_e32 v59, 0x7fffc0, v59
	v_and_b32_e32 v62, 0x7fffc0, v62
	v_and_b32_e32 v89, 0x7fffc0, v89
	v_and_b32_e32 v88, 0x7fffc0, v88
	v_and_b32_e32 v86, 0x7fffc0, v86
	v_and_b32_e32 v7, 0x7fffc0, v7
	ds_swizzle_b32 v10, v9 offset:swizzle(BROADCAST,8,0)
	ds_swizzle_b32 v11, v9 offset:swizzle(BROADCAST,8,1)
	ds_swizzle_b32 v13, v9 offset:swizzle(BROADCAST,8,3)
	ds_swizzle_b32 v12, v9 offset:swizzle(BROADCAST,8,2)
	ds_swizzle_b32 v14, v9 offset:swizzle(BROADCAST,8,4)
	ds_swizzle_b32 v15, v9 offset:swizzle(BROADCAST,8,5)
	s_waitcnt lgkmcnt(0)
	v_add_u32_e32 v10, v10, v81
	v_add_u32_e32 v11, v11, v81
	v_add_u32_e32 v13, v13, v81
	ds_swizzle_b32 v16, v9 offset:swizzle(BROADCAST,8,6)
	ds_swizzle_b32 v9, v9 offset:swizzle(BROADCAST,8,7)
	v_add_u32_e32 v12, v12, v81
	global_load_dwordx2 v[56:57], v10, s[30:31]
	global_load_dwordx2 v[52:53], v11, s[30:31]
	global_load_dwordx2 v[30:31], v12, s[30:31]
	global_load_dwordx2 v[24:25], v13, s[30:31]
	v_add_u32_e32 v10, v14, v81
	v_add_u32_e32 v11, v15, v81
	ds_swizzle_b32 v13, v8 offset:swizzle(BROADCAST,8,0)
	ds_swizzle_b32 v14, v8 offset:swizzle(BROADCAST,8,1)
	ds_swizzle_b32 v15, v8 offset:swizzle(BROADCAST,8,2)
	s_waitcnt lgkmcnt(3)
	v_add_u32_e32 v9, v9, v81
	v_add_u32_e32 v12, v16, v81
	ds_swizzle_b32 v16, v8 offset:swizzle(BROADCAST,8,3)
	global_load_dwordx2 v[54:55], v10, s[30:31]
	global_load_dwordx2 v[50:51], v11, s[30:31]
	global_load_dwordx2 v[26:27], v12, s[30:31]
	global_load_dwordx2 v[20:21], v9, s[30:31]
	s_waitcnt lgkmcnt(3)
	v_add_u32_e32 v9, v13, v81
	s_waitcnt lgkmcnt(2)
	v_add_u32_e32 v10, v14, v81
	s_waitcnt lgkmcnt(1)
	v_add_u32_e32 v11, v15, v81
	ds_swizzle_b32 v13, v8 offset:swizzle(BROADCAST,8,4)
	ds_swizzle_b32 v14, v8 offset:swizzle(BROADCAST,8,5)
	ds_swizzle_b32 v15, v8 offset:swizzle(BROADCAST,8,6)
	ds_swizzle_b32 v8, v8 offset:swizzle(BROADCAST,8,7)
	s_waitcnt lgkmcnt(4)
	v_add_u32_e32 v12, v16, v81
	global_load_dwordx2 v[28:29], v9, s[30:31]
	global_load_dwordx2 v[22:23], v10, s[30:31]
	global_load_dwordx2 v[18:19], v11, s[30:31]
	global_load_dwordx2 v[16:17], v12, s[30:31]
	s_waitcnt lgkmcnt(3)
	v_add_u32_e32 v9, v13, v81
	s_waitcnt lgkmcnt(2)
	v_add_u32_e32 v10, v14, v81
	s_waitcnt lgkmcnt(1)
	v_add_u32_e32 v11, v15, v81
	s_waitcnt lgkmcnt(0)
	v_add_u32_e32 v8, v8, v81
	global_load_dwordx2 v[14:15], v9, s[30:31]
	global_load_dwordx2 v[12:13], v10, s[30:31]
	s_nop 0
	global_load_dwordx2 v[10:11], v11, s[30:31]
	s_nop 0
	global_load_dwordx2 v[8:9], v8, s[30:31]
	v_cmp_lt_i32_e32 vcc, 16, v58
	s_cmp_lg_u64 vcc, 0
	s_cselect_b64 s[36:37], -1, 0
	v_cmp_lt_i32_e64 s[10:11], 18, v58
	v_cmp_lt_i32_e64 s[8:9], 20, v58
	v_cmp_lt_i32_e64 s[6:7], 22, v58
	s_cbranch_vccz .LBB5_42
	ds_swizzle_b32 v34, v60 offset:swizzle(BROADCAST,8,0)
	ds_swizzle_b32 v35, v60 offset:swizzle(BROADCAST,8,1)
	s_waitcnt lgkmcnt(1)
	v_add_u32_e32 v34, v34, v81
	s_waitcnt lgkmcnt(0)
	v_add_u32_e32 v38, v35, v81
	global_load_dwordx2 v[34:35], v34, s[30:31]
	s_nop 0
	global_load_dwordx2 v[38:39], v38, s[30:31]
